# v31 + redundant MoE tile-table rebuilds skipped: P11 reuses the table P10 left in LDS; P10 workgroups that skip the copy slot keep their first table
# speedup vs baseline: 1.0145x; 1.0145x over previous
.Lp10_nobuild:
	s_waitcnt lgkmcnt(0)
	s_barrier
	s_mov_b64 s[0:1], exec
	s_branch .LBB0_1788

.LBB0_1912:
	v_readlane_b32 s2, v254, 9
	v_readlane_b32 s3, v254, 10
	s_cmp_lt_i32 s2, 12
	s_cselect_b64 s[2:3], -1, 0
	s_and_b64 s[8:9], s[2:3], s[0:1]
	s_andn2_b64 vcc, exec, s[8:9]
	s_cbranch_vccnz .LBB0_2006
	s_mov_b64 s[0:1], exec
	v_readlane_b32 s2, v254, 4
	v_readlane_b32 s3, v254, 5
	s_and_b64 s[2:3], s[0:1], s[2:3]
	s_mov_b64 exec, s[2:3]
	s_branch .LBB0_1929
	s_waitcnt lgkmcnt(0)
	v_mov_b32_e32 v195, 0
	s_waitcnt vmcnt(0)
	v_lshl_add_u64 v[2:3], s[50:51], 0, v[194:195]
	v_add_co_u32_e32 v2, vcc, 0x8000, v2
	v_readlane_b32 s2, v254, 2
	s_nop 0
	v_addc_co_u32_e32 v3, vcc, 0, v3, vcc
	global_load_dword v1, v[2:3], off sc1
	v_mbcnt_lo_u32_b32 v2, -1, 0
	v_mbcnt_hi_u32_b32 v2, -1, v2
	v_and_b32_e32 v3, 64, v2
	v_add_u32_e32 v4, -1, v2
	v_cmp_lt_i32_e32 vcc, v4, v3
	v_add_u32_e32 v5, -2, v2
	v_readlane_b32 s3, v254, 3
	v_cndmask_b32_e32 v4, v4, v2, vcc
	v_lshlrev_b32_e32 v6, 2, v4
	v_cmp_lt_i32_e32 vcc, v5, v3
	v_add_u32_e32 v7, -4, v2
	v_add_u32_e32 v8, -8, v2
	v_cndmask_b32_e32 v5, v5, v2, vcc
	v_lshlrev_b32_e32 v5, 2, v5
	v_cmp_lt_i32_e32 vcc, v7, v3
	v_add_u32_e32 v9, -16, v2
	v_subrev_u32_e32 v10, 32, v2
	v_cndmask_b32_e32 v7, v7, v2, vcc
	v_cmp_lt_u32_e32 vcc, 1, v0
	v_lshlrev_b32_e32 v12, 2, v7
	s_waitcnt vmcnt(0)
	v_add_u32_e32 v4, 0xff, v1
	v_ashrrev_i32_e32 v4, 8, v4
	ds_bpermute_b32 v6, v6, v4
	s_waitcnt lgkmcnt(0)
	v_cndmask_b32_e64 v6, v6, 0, s[2:3]
	v_add_u32_e32 v11, v6, v4
	ds_bpermute_b32 v5, v5, v11
	s_waitcnt lgkmcnt(0)
	v_cndmask_b32_e32 v7, 0, v5, vcc
	v_add_u32_e32 v5, v7, v11
	ds_bpermute_b32 v11, v12, v5
	v_cmp_lt_i32_e32 vcc, v8, v3
	s_nop 1
	v_cndmask_b32_e32 v8, v8, v2, vcc
	v_cmp_lt_u32_e32 vcc, 3, v0
	v_lshlrev_b32_e32 v12, 2, v8
	s_waitcnt lgkmcnt(0)
	v_cndmask_b32_e32 v8, 0, v11, vcc
	v_add_u32_e32 v5, v8, v5
	ds_bpermute_b32 v11, v12, v5
	v_cmp_lt_i32_e32 vcc, v9, v3
	s_nop 1
	v_cndmask_b32_e32 v9, v9, v2, vcc
	v_cmp_lt_u32_e32 vcc, 7, v0
	v_lshlrev_b32_e32 v12, 2, v9
	s_waitcnt lgkmcnt(0)
	v_cndmask_b32_e32 v9, 0, v11, vcc
	v_add_u32_e32 v5, v9, v5
	ds_bpermute_b32 v11, v12, v5
	v_cmp_lt_i32_e32 vcc, v10, v3
	s_nop 1
	v_cndmask_b32_e32 v2, v10, v2, vcc
	v_cmp_lt_u32_e32 vcc, 15, v0
	v_lshlrev_b32_e32 v2, 2, v2
	s_waitcnt lgkmcnt(0)
	v_cndmask_b32_e32 v10, 0, v11, vcc
	v_add_u32_e32 v3, v10, v5
	ds_bpermute_b32 v2, v2, v3
	v_cmp_lt_u32_e32 vcc, 31, v0
	v_add_u32_e32 v5, 0, v194
	v_add_u32_e32 v12, 0x20b20, v5
	s_waitcnt lgkmcnt(0)
	v_cndmask_b32_e32 v11, 0, v2, vcc
	v_add_u32_e32 v5, v11, v3
	v_sub_u32_e32 v2, v5, v4
	v_lshlrev_b32_e32 v2, 8, v2
	v_cmp_lt_i32_e32 vcc, 0, v4
	ds_write_b32 v12, v2
	s_and_saveexec_b64 s[2:3], vcc
	s_cbranch_execz .LBB0_1927
	v_cmp_ne_u32_e32 vcc, 1, v4
	s_mov_b64 s[6:7], -1
	s_and_saveexec_b64 s[4:5], vcc
	s_cbranch_execz .LBB0_1924
	v_add_u32_e32 v2, -2, v4
	v_lshrrev_b32_e32 v3, 1, v2
	v_cmp_lt_u32_e32 vcc, 13, v2
	v_mov_b32_e32 v2, 0
	s_mov_b32 s7, 1
	v_add_u32_e32 v12, 1, v3
	s_mov_b32 s14, 0
	v_mov_b32_e32 v3, 1
	v_mov_b32_e32 v15, v2
	s_and_saveexec_b64 s[10:11], vcc
	s_cbranch_execz .LBB0_1920
	v_add_u32_e32 v2, v6, v7
	v_add3_u32 v2, v2, v8, v9
	v_add3_u32 v2, v2, v10, v11
	v_lshl_add_u32 v2, v2, 2, 0
	v_and_b32_e32 v13, -8, v12
	v_add_u32_e32 v14, 0x20000, v2
	s_mov_b64 s[12:13], 0
	s_mov_b32 s6, 0
